# MoE K-loops stagger variant: odd waves (instead of waves 4-7) run the weight-tile block first
# speedup vs baseline: 1.0203x; 1.0074x over previous
.LBB0_1013:
	s_or_b64 exec, exec, s[34:35]
	s_lshl_b64 s[34:35], s[10:11], 22
	s_add_u32 s10, s12, s34
	s_addc_u32 s52, s13, s35
	s_lshl_b32 s34, s36, 9
	s_lshl_b32 s35, s46, 6
	s_sub_i32 s34, s35, s34
	s_ashr_i32 s35, s34, 31
	s_lshl_b64 s[36:37], s[34:35], 2
	s_add_u32 s36, s10, s36
	s_addc_u32 s37, s52, s37
	v_or_b32_e32 v146, v3, v1
	s_waitcnt lgkmcnt(0)
	v_readfirstlane_b32 s51, v2
	v_lshl_add_u64 v[2:3], s[36:37], 0, v[152:153]
	v_lshl_add_u64 v[156:157], v[2:3], 0, v[148:149]
	s_mov_b64 s[36:37], -1
	s_cmp_ge_i32 s38, s50
	v_lshl_add_u64 v[132:133], v[156:157], 0, s[22:23]
	v_lshl_add_u64 v[130:131], v[156:157], 0, s[24:25]
	v_lshl_add_u64 v[134:135], v[156:157], 0, s[26:27]
	v_lshl_add_u64 v[138:139], v[156:157], 0, s[28:29]
	v_lshl_add_u64 v[142:143], v[156:157], 0, s[30:31]
	s_cbranch_scc0 .LBB0_1017
	global_load_dwordx4 v[2:5], v[156:157], off sc1 nt
	s_mov_b32 m0, s39
	global_load_dwordx4 v[6:9], v[132:133], off sc1 nt
	v_lshl_add_u64 v[50:51], s[14:15], 0, v[146:147]
	global_load_lds_dwordx4 v146, s[14:15]
	global_load_dwordx4 v[34:37], v[130:131], off sc1 nt
	global_load_dwordx4 v[38:41], v[134:135], off sc1 nt
	s_mov_b32 m0, s40
	s_nop 0
	global_load_lds_dwordx4 v146, s[16:17]
	s_waitcnt vmcnt(4)
	s_nop 0
	v_cvt_pk_bf16_f32 v2, v2, v6
	ds_write_b32 v169, v2 offset:49152
	v_cvt_pk_bf16_f32 v2, v3, v7
	ds_write_b32 v169, v2 offset:49216
	v_cvt_pk_bf16_f32 v2, v4, v8
	ds_write_b32 v169, v2 offset:49280
	v_cvt_pk_bf16_f32 v2, v5, v9
	ds_write_b32 v169, v2 offset:49344
	global_load_dwordx4 v[42:45], v[138:139], off sc1 nt
	global_load_dwordx4 v[46:49], v[142:143], off sc1 nt
	s_waitcnt vmcnt(5)
	s_mov_b32 m0, s41
	s_waitcnt lgkmcnt(0)
	s_barrier
	global_load_lds_dwordx4 v146, s[18:19]
	v_mov_b32_e32 v2, 0
	s_mov_b32 s37, -2
	s_movk_i32 s36, 0x80
	v_mov_b32_e32 v3, v2
	v_mov_b32_e32 v4, v2
	v_mov_b32_e32 v5, v2
	v_mov_b32_e32 v6, v2
	v_mov_b32_e32 v7, v2
	v_mov_b32_e32 v8, v2
	v_mov_b32_e32 v9, v2
	v_mov_b32_e32 v10, v2
	v_mov_b32_e32 v11, v2
	v_mov_b32_e32 v12, v2
	v_mov_b32_e32 v13, v2
	v_mov_b32_e32 v14, v2
	v_mov_b32_e32 v15, v2
	v_mov_b32_e32 v16, v2
	v_mov_b32_e32 v17, v2
	v_mov_b32_e32 v66, v2
	v_mov_b32_e32 v67, v2
	v_mov_b32_e32 v68, v2
	v_mov_b32_e32 v69, v2
	v_mov_b32_e32 v70, v2
	v_mov_b32_e32 v71, v2
	v_mov_b32_e32 v72, v2
	v_mov_b32_e32 v73, v2
	v_mov_b32_e32 v74, v2
	v_mov_b32_e32 v75, v2
	v_mov_b32_e32 v76, v2
	v_mov_b32_e32 v77, v2
	v_mov_b32_e32 v78, v2
	v_mov_b32_e32 v79, v2
	v_mov_b32_e32 v80, v2
	v_mov_b32_e32 v81, v2
	v_mov_b32_e32 v18, v2
	v_mov_b32_e32 v19, v2
	v_mov_b32_e32 v20, v2
	v_mov_b32_e32 v21, v2
	v_mov_b32_e32 v22, v2
	v_mov_b32_e32 v23, v2
	v_mov_b32_e32 v24, v2
	v_mov_b32_e32 v25, v2
	v_mov_b32_e32 v26, v2
	v_mov_b32_e32 v27, v2
	v_mov_b32_e32 v28, v2
	v_mov_b32_e32 v29, v2
	v_mov_b32_e32 v30, v2
	v_mov_b32_e32 v31, v2
	v_mov_b32_e32 v32, v2
	v_mov_b32_e32 v33, v2
	v_mov_b32_e32 v114, v2
	v_mov_b32_e32 v115, v2
	v_mov_b32_e32 v116, v2
	v_mov_b32_e32 v117, v2
	v_mov_b32_e32 v118, v2
	v_mov_b32_e32 v119, v2
	v_mov_b32_e32 v120, v2
	v_mov_b32_e32 v121, v2
	v_mov_b32_e32 v122, v2
	v_mov_b32_e32 v123, v2
	v_mov_b32_e32 v124, v2
	v_mov_b32_e32 v125, v2
	v_mov_b32_e32 v126, v2
	v_mov_b32_e32 v127, v2
	v_mov_b32_e32 v128, v2
	v_mov_b32_e32 v129, v2
	v_readfirstlane_b32 s98, v250
	s_bitcmp1_b32 s98, 6
	s_cbranch_scc1 .Lmoe_B_1015

.LBB0_1017:
	v_mov_b32_e32 v97, 0
	s_and_b64 vcc, exec, s[36:37]
	v_mov_b32_e32 v96, v97
	v_mov_b32_e32 v95, v97
	v_mov_b32_e32 v94, v97
	v_mov_b32_e32 v93, v97
	v_mov_b32_e32 v92, v97
	v_mov_b32_e32 v91, v97
	v_mov_b32_e32 v90, v97
	v_mov_b32_e32 v89, v97
	v_mov_b32_e32 v88, v97
	v_mov_b32_e32 v87, v97
	v_mov_b32_e32 v86, v97
	v_mov_b32_e32 v85, v97
	v_mov_b32_e32 v84, v97
	v_mov_b32_e32 v83, v97
	v_mov_b32_e32 v82, v97
	v_mov_b32_e32 v65, v97
	v_mov_b32_e32 v64, v97
	v_mov_b32_e32 v63, v97
	v_mov_b32_e32 v62, v97
	v_mov_b32_e32 v61, v97
	v_mov_b32_e32 v60, v97
	v_mov_b32_e32 v59, v97
	v_mov_b32_e32 v58, v97
	v_mov_b32_e32 v57, v97
	v_mov_b32_e32 v56, v97
	v_mov_b32_e32 v55, v97
	v_mov_b32_e32 v54, v97
	v_mov_b32_e32 v53, v97
	v_mov_b32_e32 v52, v97
	v_mov_b32_e32 v51, v97
	v_mov_b32_e32 v50, v97
	v_mov_b32_e32 v113, v97
	v_mov_b32_e32 v112, v97
	v_mov_b32_e32 v111, v97
	v_mov_b32_e32 v110, v97
	v_mov_b32_e32 v109, v97
	v_mov_b32_e32 v108, v97
	v_mov_b32_e32 v107, v97
	v_mov_b32_e32 v106, v97
	v_mov_b32_e32 v105, v97
	v_mov_b32_e32 v104, v97
	v_mov_b32_e32 v103, v97
	v_mov_b32_e32 v102, v97
	v_mov_b32_e32 v101, v97
	v_mov_b32_e32 v100, v97
	v_mov_b32_e32 v99, v97
	v_mov_b32_e32 v98, v97
	v_mov_b32_e32 v49, v97
	v_mov_b32_e32 v48, v97
	v_mov_b32_e32 v47, v97
	v_mov_b32_e32 v46, v97
	v_mov_b32_e32 v45, v97
	v_mov_b32_e32 v44, v97
	v_mov_b32_e32 v43, v97
	v_mov_b32_e32 v42, v97
	v_mov_b32_e32 v41, v97
	v_mov_b32_e32 v40, v97
	v_mov_b32_e32 v39, v97
	v_mov_b32_e32 v38, v97
	v_mov_b32_e32 v37, v97
	v_mov_b32_e32 v36, v97
	v_mov_b32_e32 v35, v97
	v_mov_b32_e32 v34, v97
	s_cbranch_vccz .LBB0_1021
	global_load_dwordx4 v[2:5], v[156:157], off sc1 nt
	s_mov_b32 m0, s39
	global_load_dwordx4 v[6:9], v[132:133], off sc1 nt
	v_or_b32_e32 v158, v136, v1
	global_load_lds_dwordx4 v146, s[14:15]
	s_mov_b32 m0, s42
	v_mov_b32_e32 v159, v147
	global_load_lds_dwordx4 v158, s[14:15]
	global_load_dwordx4 v[130:133], v[130:131], off sc1 nt
	global_load_dwordx4 v[134:137], v[134:135], off sc1 nt
	s_mov_b32 m0, s40
	s_nop 0
	global_load_lds_dwordx4 v146, s[16:17]
	s_mov_b32 m0, s43
	s_nop 0
	global_load_lds_dwordx4 v158, s[16:17]
	s_waitcnt vmcnt(6)
	s_nop 0
	v_cvt_pk_bf16_f32 v2, v2, v6
	ds_write_b32 v169, v2 offset:49152
	v_cvt_pk_bf16_f32 v2, v3, v7
	ds_write_b32 v169, v2 offset:49216
	v_cvt_pk_bf16_f32 v2, v4, v8
	ds_write_b32 v169, v2 offset:49280
	v_cvt_pk_bf16_f32 v2, v5, v9
	ds_write_b32 v169, v2 offset:49344
	global_load_dwordx4 v[138:141], v[138:139], off sc1 nt
	global_load_dwordx4 v[142:145], v[142:143], off sc1 nt
	s_waitcnt vmcnt(6)
	s_mov_b32 m0, s41
	s_waitcnt lgkmcnt(0)
	s_barrier
	global_load_lds_dwordx4 v146, s[18:19]
	s_mov_b32 m0, s44
	v_mov_b32_e32 v34, 0
	global_load_lds_dwordx4 v158, s[18:19]
	s_mov_b32 s37, -2
	s_movk_i32 s36, 0x80
	v_mov_b32_e32 v35, v34
	v_mov_b32_e32 v36, v34
	v_mov_b32_e32 v37, v34
	v_mov_b32_e32 v38, v34
	v_mov_b32_e32 v39, v34
	v_mov_b32_e32 v40, v34
	v_mov_b32_e32 v41, v34
	v_mov_b32_e32 v42, v34
	v_mov_b32_e32 v43, v34
	v_mov_b32_e32 v44, v34
	v_mov_b32_e32 v45, v34
	v_mov_b32_e32 v46, v34
	v_mov_b32_e32 v47, v34
	v_mov_b32_e32 v48, v34
	v_mov_b32_e32 v49, v34
	v_mov_b32_e32 v98, v34
	v_mov_b32_e32 v99, v34
	v_mov_b32_e32 v100, v34
	v_mov_b32_e32 v101, v34
	v_mov_b32_e32 v102, v34
	v_mov_b32_e32 v103, v34
	v_mov_b32_e32 v104, v34
	v_mov_b32_e32 v105, v34
	v_mov_b32_e32 v106, v34
	v_mov_b32_e32 v107, v34
	v_mov_b32_e32 v108, v34
	v_mov_b32_e32 v109, v34
	v_mov_b32_e32 v110, v34
	v_mov_b32_e32 v111, v34
	v_mov_b32_e32 v112, v34
	v_mov_b32_e32 v113, v34
	v_mov_b32_e32 v50, v34
	v_mov_b32_e32 v51, v34
	v_mov_b32_e32 v52, v34
	v_mov_b32_e32 v53, v34
	v_mov_b32_e32 v54, v34
	v_mov_b32_e32 v55, v34
	v_mov_b32_e32 v56, v34
	v_mov_b32_e32 v57, v34
	v_mov_b32_e32 v58, v34
	v_mov_b32_e32 v59, v34
	v_mov_b32_e32 v60, v34
	v_mov_b32_e32 v61, v34
	v_mov_b32_e32 v62, v34
	v_mov_b32_e32 v63, v34
	v_mov_b32_e32 v64, v34
	v_mov_b32_e32 v65, v34
	v_mov_b32_e32 v82, v34
	v_mov_b32_e32 v83, v34
	v_mov_b32_e32 v84, v34
	v_mov_b32_e32 v85, v34
	v_mov_b32_e32 v86, v34
	v_mov_b32_e32 v87, v34
	v_mov_b32_e32 v88, v34
	v_mov_b32_e32 v89, v34
	v_mov_b32_e32 v90, v34
	v_mov_b32_e32 v91, v34
	v_mov_b32_e32 v92, v34
	v_mov_b32_e32 v93, v34
	v_mov_b32_e32 v94, v34
	v_mov_b32_e32 v95, v34
	v_mov_b32_e32 v96, v34
	v_mov_b32_e32 v97, v34
	v_mov_b32_e32 v2, v34
	v_mov_b32_e32 v3, v34
	v_mov_b32_e32 v4, v34
	v_mov_b32_e32 v5, v34
	v_mov_b32_e32 v6, v34
	v_mov_b32_e32 v7, v34
	v_mov_b32_e32 v8, v34
	v_mov_b32_e32 v9, v34
	v_mov_b32_e32 v10, v34
	v_mov_b32_e32 v11, v34
	v_mov_b32_e32 v12, v34
	v_mov_b32_e32 v13, v34
	v_mov_b32_e32 v14, v34
	v_mov_b32_e32 v15, v34
	v_mov_b32_e32 v16, v34
	v_mov_b32_e32 v17, v34
	v_mov_b32_e32 v66, v34
	v_mov_b32_e32 v67, v34
	v_mov_b32_e32 v68, v34
	v_mov_b32_e32 v69, v34
	v_mov_b32_e32 v70, v34
	v_mov_b32_e32 v71, v34
	v_mov_b32_e32 v72, v34
	v_mov_b32_e32 v73, v34
	v_mov_b32_e32 v74, v34
	v_mov_b32_e32 v75, v34
	v_mov_b32_e32 v76, v34
	v_mov_b32_e32 v77, v34
	v_mov_b32_e32 v78, v34
	v_mov_b32_e32 v79, v34
	v_mov_b32_e32 v80, v34
	v_mov_b32_e32 v81, v34
	v_mov_b32_e32 v18, v34
	v_mov_b32_e32 v19, v34
	v_mov_b32_e32 v20, v34
	v_mov_b32_e32 v21, v34
	v_mov_b32_e32 v22, v34
	v_mov_b32_e32 v23, v34
	v_mov_b32_e32 v24, v34
	v_mov_b32_e32 v25, v34
	v_mov_b32_e32 v26, v34
	v_mov_b32_e32 v27, v34
	v_mov_b32_e32 v28, v34
	v_mov_b32_e32 v29, v34
	v_mov_b32_e32 v30, v34
	v_mov_b32_e32 v31, v34
	v_mov_b32_e32 v32, v34
	v_mov_b32_e32 v33, v34
	v_mov_b32_e32 v114, v34
	v_mov_b32_e32 v115, v34
	v_mov_b32_e32 v116, v34
	v_mov_b32_e32 v117, v34
	v_mov_b32_e32 v118, v34
	v_mov_b32_e32 v119, v34
	v_mov_b32_e32 v120, v34
	v_mov_b32_e32 v121, v34
	v_mov_b32_e32 v122, v34
	v_mov_b32_e32 v123, v34
	v_mov_b32_e32 v124, v34
	v_mov_b32_e32 v125, v34
	v_mov_b32_e32 v126, v34
	v_mov_b32_e32 v127, v34
	v_mov_b32_e32 v128, v34
	v_mov_b32_e32 v129, v34
	v_readfirstlane_b32 s98, v250
	s_bitcmp1_b32 s98, 6
	s_cbranch_scc1 .Lmoe_B_1019

.LBB0_1084:
	s_add_i32 s31, s30, s34
	s_lshl_b32 s35, s31, 2
	s_add_i32 s35, s35, 0
	s_add_i32 s35, s35, 0x20000
	v_mov_b32_e32 v2, s35
	ds_read_b32 v2, v2
	s_waitcnt lgkmcnt(0)
	v_readfirstlane_b32 s35, v2
	s_cmp_gt_i32 s35, s10
	s_cselect_b32 s34, s34, s31
	s_lshr_b32 s31, s30, 1
	s_cmp_lt_u32 s30, 2
	s_mov_b32 s30, s31
	s_cbranch_scc0 .LBB0_1084
	s_lshl_b32 s30, s34, 2
	s_add_i32 s30, s30, 0
	s_add_i32 s30, s30, 0x20000
	v_mov_b32_e32 v4, s30
	ds_read2_b32 v[2:3], v4 offset1:80
	ds_read_b32 v4, v4 offset:640
	s_mov_b32 s35, s11
	s_waitcnt lgkmcnt(1)
	v_readfirstlane_b32 s30, v2
	s_sub_i32 s30, s10, s30
	v_readfirstlane_b32 s31, v3
	s_lshl_b32 s47, s30, 9
	s_waitcnt lgkmcnt(0)
	v_readfirstlane_b32 s49, v4
	s_sub_i32 s30, s31, s47
	s_add_i32 s49, s49, s47
	s_min_i32 s48, s30, 0x200
	s_lshl_b64 s[30:31], s[34:35], 22
	s_add_u32 s35, s6, s30
	s_addc_u32 s50, s7, s31
	s_lshl_b32 s10, s10, 11
	s_lshl_b32 s30, s46, 7
	s_sub_i32 s30, s30, s10
	s_ashr_i32 s31, s30, 31
	v_cmp_gt_i32_e32 vcc, s48, v0
	s_lshl_b64 s[36:37], s[30:31], 2
	s_add_u32 s36, s35, s36
	v_cndmask_b32_e32 v2, 0, v0, vcc
	v_add_u32_e32 v2, s49, v2
	s_addc_u32 s37, s50, s37
	v_lshl_or_b32 v146, v2, 9, v1
	v_lshl_add_u64 v[2:3], s[36:37], 0, v[152:153]
	v_lshl_add_u64 v[154:155], v[2:3], 0, v[148:149]
	s_mov_b64 s[36:37], -1
	s_cmp_ge_i32 s38, s48
	v_lshl_add_u64 v[132:133], v[154:155], 0, s[20:21]
	v_lshl_add_u64 v[130:131], v[154:155], 0, s[22:23]
	v_lshl_add_u64 v[134:135], v[154:155], 0, s[24:25]
	v_lshl_add_u64 v[138:139], v[154:155], 0, s[26:27]
	v_lshl_add_u64 v[142:143], v[154:155], 0, s[28:29]
	s_cbranch_scc0 .LBB0_1089
	global_load_dwordx4 v[2:5], v[154:155], off sc1 nt
	s_mov_b32 m0, s39
	global_load_dwordx4 v[6:9], v[132:133], off sc1 nt
	v_lshl_add_u64 v[82:83], s[12:13], 0, v[146:147]
	global_load_lds_dwordx4 v146, s[12:13]
	global_load_dwordx4 v[66:69], v[130:131], off sc1 nt
	global_load_dwordx4 v[70:73], v[134:135], off sc1 nt
	s_mov_b32 m0, s40
	s_nop 0
	global_load_lds_dwordx4 v146, s[14:15]
	s_waitcnt vmcnt(4)
	s_nop 0
	v_cvt_pk_bf16_f32 v2, v2, v6
	ds_write_b32 v167, v2 offset:49152
	v_cvt_pk_bf16_f32 v2, v3, v7
	ds_write_b32 v167, v2 offset:49216
	v_cvt_pk_bf16_f32 v2, v4, v8
	ds_write_b32 v167, v2 offset:49280
	v_cvt_pk_bf16_f32 v2, v5, v9
	ds_write_b32 v167, v2 offset:49344
	global_load_dwordx4 v[74:77], v[138:139], off sc1 nt
	global_load_dwordx4 v[78:81], v[142:143], off sc1 nt
	s_waitcnt vmcnt(5)
	s_mov_b32 m0, s41
	s_waitcnt lgkmcnt(0)
	s_barrier
	global_load_lds_dwordx4 v146, s[16:17]
	v_mov_b32_e32 v2, 0
	s_mov_b32 s36, -2
	s_movk_i32 s35, 0x80
	v_mov_b32_e32 v3, v2
	v_mov_b32_e32 v4, v2
	v_mov_b32_e32 v5, v2
	v_mov_b32_e32 v6, v2
	v_mov_b32_e32 v7, v2
	v_mov_b32_e32 v8, v2
	v_mov_b32_e32 v9, v2
	v_mov_b32_e32 v10, v2
	v_mov_b32_e32 v11, v2
	v_mov_b32_e32 v12, v2
	v_mov_b32_e32 v13, v2
	v_mov_b32_e32 v14, v2
	v_mov_b32_e32 v15, v2
	v_mov_b32_e32 v16, v2
	v_mov_b32_e32 v17, v2
	v_mov_b32_e32 v18, v2
	v_mov_b32_e32 v19, v2
	v_mov_b32_e32 v20, v2
	v_mov_b32_e32 v21, v2
	v_mov_b32_e32 v22, v2
	v_mov_b32_e32 v23, v2
	v_mov_b32_e32 v24, v2
	v_mov_b32_e32 v25, v2
	v_mov_b32_e32 v26, v2
	v_mov_b32_e32 v27, v2
	v_mov_b32_e32 v28, v2
	v_mov_b32_e32 v29, v2
	v_mov_b32_e32 v30, v2
	v_mov_b32_e32 v31, v2
	v_mov_b32_e32 v32, v2
	v_mov_b32_e32 v33, v2
	v_mov_b32_e32 v34, v2
	v_mov_b32_e32 v35, v2
	v_mov_b32_e32 v36, v2
	v_mov_b32_e32 v37, v2
	v_mov_b32_e32 v38, v2
	v_mov_b32_e32 v39, v2
	v_mov_b32_e32 v40, v2
	v_mov_b32_e32 v41, v2
	v_mov_b32_e32 v42, v2
	v_mov_b32_e32 v43, v2
	v_mov_b32_e32 v44, v2
	v_mov_b32_e32 v45, v2
	v_mov_b32_e32 v46, v2
	v_mov_b32_e32 v47, v2
	v_mov_b32_e32 v48, v2
	v_mov_b32_e32 v49, v2
	v_mov_b32_e32 v50, v2
	v_mov_b32_e32 v51, v2
	v_mov_b32_e32 v52, v2
	v_mov_b32_e32 v53, v2
	v_mov_b32_e32 v54, v2
	v_mov_b32_e32 v55, v2
	v_mov_b32_e32 v56, v2
	v_mov_b32_e32 v57, v2
	v_mov_b32_e32 v58, v2
	v_mov_b32_e32 v59, v2
	v_mov_b32_e32 v60, v2
	v_mov_b32_e32 v61, v2
	v_mov_b32_e32 v62, v2
	v_mov_b32_e32 v63, v2
	v_mov_b32_e32 v64, v2
	v_mov_b32_e32 v65, v2
	v_readfirstlane_b32 s98, v250
	s_bitcmp1_b32 s98, 6
	s_cbranch_scc1 .Lmoe_B_1087

.LBB0_1089:
	v_mov_b32_e32 v129, 0
	s_and_b64 vcc, exec, s[36:37]
	v_mov_b32_e32 v128, v129
	v_mov_b32_e32 v127, v129
	v_mov_b32_e32 v126, v129
	v_mov_b32_e32 v125, v129
	v_mov_b32_e32 v124, v129
	v_mov_b32_e32 v123, v129
	v_mov_b32_e32 v122, v129
	v_mov_b32_e32 v121, v129
	v_mov_b32_e32 v120, v129
	v_mov_b32_e32 v119, v129
	v_mov_b32_e32 v118, v129
	v_mov_b32_e32 v117, v129
	v_mov_b32_e32 v116, v129
	v_mov_b32_e32 v115, v129
	v_mov_b32_e32 v114, v129
	v_mov_b32_e32 v113, v129
	v_mov_b32_e32 v112, v129
	v_mov_b32_e32 v111, v129
	v_mov_b32_e32 v110, v129
	v_mov_b32_e32 v109, v129
	v_mov_b32_e32 v108, v129
	v_mov_b32_e32 v107, v129
	v_mov_b32_e32 v106, v129
	v_mov_b32_e32 v105, v129
	v_mov_b32_e32 v104, v129
	v_mov_b32_e32 v103, v129
	v_mov_b32_e32 v102, v129
	v_mov_b32_e32 v101, v129
	v_mov_b32_e32 v100, v129
	v_mov_b32_e32 v99, v129
	v_mov_b32_e32 v98, v129
	v_mov_b32_e32 v97, v129
	v_mov_b32_e32 v96, v129
	v_mov_b32_e32 v95, v129
	v_mov_b32_e32 v94, v129
	v_mov_b32_e32 v93, v129
	v_mov_b32_e32 v92, v129
	v_mov_b32_e32 v91, v129
	v_mov_b32_e32 v90, v129
	v_mov_b32_e32 v89, v129
	v_mov_b32_e32 v88, v129
	v_mov_b32_e32 v87, v129
	v_mov_b32_e32 v86, v129
	v_mov_b32_e32 v85, v129
	v_mov_b32_e32 v84, v129
	v_mov_b32_e32 v83, v129
	v_mov_b32_e32 v82, v129
	v_mov_b32_e32 v81, v129
	v_mov_b32_e32 v80, v129
	v_mov_b32_e32 v79, v129
	v_mov_b32_e32 v78, v129
	v_mov_b32_e32 v77, v129
	v_mov_b32_e32 v76, v129
	v_mov_b32_e32 v75, v129
	v_mov_b32_e32 v74, v129
	v_mov_b32_e32 v73, v129
	v_mov_b32_e32 v72, v129
	v_mov_b32_e32 v71, v129
	v_mov_b32_e32 v70, v129
	v_mov_b32_e32 v69, v129
	v_mov_b32_e32 v68, v129
	v_mov_b32_e32 v67, v129
	v_mov_b32_e32 v66, v129
	s_cbranch_vccz .LBB0_1093
	v_cmp_gt_i32_e32 vcc, s48, v165
	s_mov_b32 m0, s39
	v_mov_b32_e32 v157, v147
	v_cndmask_b32_e32 v2, 0, v165, vcc
	v_add_u32_e32 v2, s49, v2
	v_lshl_or_b32 v156, v2, 9, v1
	global_load_dwordx4 v[2:5], v[154:155], off sc1 nt
	global_load_dwordx4 v[6:9], v[132:133], off sc1 nt
	global_load_lds_dwordx4 v146, s[12:13]
	s_mov_b32 m0, s42
	s_nop 0
	global_load_lds_dwordx4 v156, s[12:13]
	global_load_dwordx4 v[130:133], v[130:131], off sc1 nt
	global_load_dwordx4 v[134:137], v[134:135], off sc1 nt
	s_mov_b32 m0, s40
	s_nop 0
	global_load_lds_dwordx4 v146, s[14:15]
	s_mov_b32 m0, s43
	s_nop 0
	global_load_lds_dwordx4 v156, s[14:15]
	s_waitcnt vmcnt(6)
	s_nop 0
	v_cvt_pk_bf16_f32 v2, v2, v6
	ds_write_b32 v167, v2 offset:49152
	v_cvt_pk_bf16_f32 v2, v3, v7
	ds_write_b32 v167, v2 offset:49216
	v_cvt_pk_bf16_f32 v2, v4, v8
	ds_write_b32 v167, v2 offset:49280
	v_cvt_pk_bf16_f32 v2, v5, v9
	ds_write_b32 v167, v2 offset:49344
	global_load_dwordx4 v[138:141], v[138:139], off sc1 nt
	global_load_dwordx4 v[142:145], v[142:143], off sc1 nt
	s_waitcnt vmcnt(6)
	s_mov_b32 m0, s41
	s_waitcnt lgkmcnt(0)
	s_barrier
	global_load_lds_dwordx4 v146, s[16:17]
	s_mov_b32 m0, s44
	v_mov_b32_e32 v66, 0
	global_load_lds_dwordx4 v156, s[16:17]
	s_mov_b32 s36, -2
	s_movk_i32 s35, 0x80
	v_mov_b32_e32 v67, v66
	v_mov_b32_e32 v68, v66
	v_mov_b32_e32 v69, v66
	v_mov_b32_e32 v70, v66
	v_mov_b32_e32 v71, v66
	v_mov_b32_e32 v72, v66
	v_mov_b32_e32 v73, v66
	v_mov_b32_e32 v74, v66
	v_mov_b32_e32 v75, v66
	v_mov_b32_e32 v76, v66
	v_mov_b32_e32 v77, v66
	v_mov_b32_e32 v78, v66
	v_mov_b32_e32 v79, v66
	v_mov_b32_e32 v80, v66
	v_mov_b32_e32 v81, v66
	v_mov_b32_e32 v82, v66
	v_mov_b32_e32 v83, v66
	v_mov_b32_e32 v84, v66
	v_mov_b32_e32 v85, v66
	v_mov_b32_e32 v86, v66
	v_mov_b32_e32 v87, v66
	v_mov_b32_e32 v88, v66
	v_mov_b32_e32 v89, v66
	v_mov_b32_e32 v90, v66
	v_mov_b32_e32 v91, v66
	v_mov_b32_e32 v92, v66
	v_mov_b32_e32 v93, v66
	v_mov_b32_e32 v94, v66
	v_mov_b32_e32 v95, v66
	v_mov_b32_e32 v96, v66
	v_mov_b32_e32 v97, v66
	v_mov_b32_e32 v98, v66
	v_mov_b32_e32 v99, v66
	v_mov_b32_e32 v100, v66
	v_mov_b32_e32 v101, v66
	v_mov_b32_e32 v102, v66
	v_mov_b32_e32 v103, v66
	v_mov_b32_e32 v104, v66
	v_mov_b32_e32 v105, v66
	v_mov_b32_e32 v106, v66
	v_mov_b32_e32 v107, v66
	v_mov_b32_e32 v108, v66
	v_mov_b32_e32 v109, v66
	v_mov_b32_e32 v110, v66
	v_mov_b32_e32 v111, v66
	v_mov_b32_e32 v112, v66
	v_mov_b32_e32 v113, v66
	v_mov_b32_e32 v114, v66
	v_mov_b32_e32 v115, v66
	v_mov_b32_e32 v116, v66
	v_mov_b32_e32 v117, v66
	v_mov_b32_e32 v118, v66
	v_mov_b32_e32 v119, v66
	v_mov_b32_e32 v120, v66
	v_mov_b32_e32 v121, v66
	v_mov_b32_e32 v122, v66
	v_mov_b32_e32 v123, v66
	v_mov_b32_e32 v124, v66
	v_mov_b32_e32 v125, v66
	v_mov_b32_e32 v126, v66
	v_mov_b32_e32 v127, v66
	v_mov_b32_e32 v128, v66
	v_mov_b32_e32 v129, v66
	v_mov_b32_e32 v2, v66
	v_mov_b32_e32 v3, v66
	v_mov_b32_e32 v4, v66
	v_mov_b32_e32 v5, v66
	v_mov_b32_e32 v6, v66
	v_mov_b32_e32 v7, v66
	v_mov_b32_e32 v8, v66
	v_mov_b32_e32 v9, v66
	v_mov_b32_e32 v10, v66
	v_mov_b32_e32 v11, v66
	v_mov_b32_e32 v12, v66
	v_mov_b32_e32 v13, v66
	v_mov_b32_e32 v14, v66
	v_mov_b32_e32 v15, v66
	v_mov_b32_e32 v16, v66
	v_mov_b32_e32 v17, v66
	v_mov_b32_e32 v18, v66
	v_mov_b32_e32 v19, v66
	v_mov_b32_e32 v20, v66
	v_mov_b32_e32 v21, v66
	v_mov_b32_e32 v22, v66
	v_mov_b32_e32 v23, v66
	v_mov_b32_e32 v24, v66
	v_mov_b32_e32 v25, v66
	v_mov_b32_e32 v26, v66
	v_mov_b32_e32 v27, v66
	v_mov_b32_e32 v28, v66
	v_mov_b32_e32 v29, v66
	v_mov_b32_e32 v30, v66
	v_mov_b32_e32 v31, v66
	v_mov_b32_e32 v32, v66
	v_mov_b32_e32 v33, v66
	v_mov_b32_e32 v34, v66
	v_mov_b32_e32 v35, v66
	v_mov_b32_e32 v36, v66
	v_mov_b32_e32 v37, v66
	v_mov_b32_e32 v38, v66
	v_mov_b32_e32 v39, v66
	v_mov_b32_e32 v40, v66
	v_mov_b32_e32 v41, v66
	v_mov_b32_e32 v42, v66
	v_mov_b32_e32 v43, v66
	v_mov_b32_e32 v44, v66
	v_mov_b32_e32 v45, v66
	v_mov_b32_e32 v46, v66
	v_mov_b32_e32 v47, v66
	v_mov_b32_e32 v48, v66
	v_mov_b32_e32 v49, v66
	v_mov_b32_e32 v50, v66
	v_mov_b32_e32 v51, v66
	v_mov_b32_e32 v52, v66
	v_mov_b32_e32 v53, v66
	v_mov_b32_e32 v54, v66
	v_mov_b32_e32 v55, v66
	v_mov_b32_e32 v56, v66
	v_mov_b32_e32 v57, v66
	v_mov_b32_e32 v58, v66
	v_mov_b32_e32 v59, v66
	v_mov_b32_e32 v60, v66
	v_mov_b32_e32 v61, v66
	v_mov_b32_e32 v62, v66
	v_mov_b32_e32 v63, v66
	v_mov_b32_e32 v64, v66
	v_mov_b32_e32 v65, v66
	v_readfirstlane_b32 s98, v250
	s_bitcmp1_b32 s98, 6
	s_cbranch_scc1 .Lmoe_B_1091
